# prologue weight-conversion stores made write-through streaming (sc1 nt) on top of the phase-F DPP rewrite
# speedup vs baseline: 1.0121x; 1.0121x over previous
.LBB0_8:
	s_or_b64 exec, exec, s[4:5]
	s_waitcnt vmcnt(0)
	v_mul_f32_e32 v6, 0x42000000, v6
	v_mul_f32_e32 v2, 0x42000000, v2
	v_mov_b32_e32 v75, v71
	v_cvt_pk_fp8_f32 v75, v6, v2
	v_mul_f32_e32 v2, 0x42000000, v7
	v_mul_f32_e32 v3, 0x42000000, v3
	v_mov_b32_e32 v6, v71
	v_cvt_pk_fp8_f32 v6, v2, v3
	v_mul_f32_e32 v2, 0x42000000, v15
	v_mul_f32_e32 v3, 0x42000000, v11
	v_mul_f32_e32 v14, 0x42000000, v14
	v_cvt_pk_fp8_f32 v6, v2, v3 op_sel:[0,0,1]
	v_mul_f32_e32 v2, 0x42000000, v8
	v_mul_f32_e32 v3, 0x42000000, v4
	v_mov_b32_e32 v8, v71
	v_cvt_pk_fp8_f32 v8, v2, v3
	v_mul_f32_e32 v2, 0x42000000, v9
	v_mul_f32_e32 v3, 0x42000000, v5
	v_mov_b32_e32 v5, v71
	v_cvt_pk_fp8_f32 v5, v2, v3
	v_mul_f32_e32 v2, 0x42000000, v17
	v_mul_f32_e32 v3, 0x42000000, v13
	v_mul_f32_e32 v10, 0x42000000, v10
	v_cvt_pk_fp8_f32 v5, v2, v3 op_sel:[0,0,1]
	v_mul_f32_e32 v2, 0x42000000, v22
	v_mul_f32_e32 v3, 0x42000000, v18
	v_mov_b32_e32 v9, v71
	v_cvt_pk_fp8_f32 v75, v14, v10 op_sel:[0,0,1]
	v_cvt_pk_fp8_f32 v9, v2, v3
	v_mul_f32_e32 v2, 0x42000000, v23
	v_mul_f32_e32 v3, 0x42000000, v19
	v_mov_b32_e32 v10, v71
	v_cvt_pk_fp8_f32 v10, v2, v3
	v_mul_f32_e32 v2, 0x42000000, v31
	v_mul_f32_e32 v3, 0x42000000, v27
	v_mov_b32_e32 v11, v71
	v_cvt_pk_fp8_f32 v10, v2, v3 op_sel:[0,0,1]
	v_mul_f32_e32 v2, 0x42000000, v24
	v_mul_f32_e32 v3, 0x42000000, v20
	v_mul_f32_e32 v4, 0x42000000, v16
	v_mul_f32_e32 v7, 0x42000000, v12
	v_cvt_pk_fp8_f32 v11, v2, v3
	v_mul_f32_e32 v2, 0x42000000, v25
	v_mul_f32_e32 v3, 0x42000000, v21
	v_mov_b32_e32 v12, v71
	v_cvt_pk_fp8_f32 v8, v4, v7 op_sel:[0,0,1]
	v_mul_f32_e32 v4, 0x42000000, v30
	v_mul_f32_e32 v7, 0x42000000, v26
	v_cvt_pk_fp8_f32 v12, v2, v3
	v_cvt_pk_fp8_f32 v9, v4, v7 op_sel:[0,0,1]
	v_mul_f32_e32 v4, 0x42000000, v32
	v_mul_f32_e32 v7, 0x42000000, v28
	v_cvt_pk_fp8_f32 v11, v4, v7 op_sel:[0,0,1]
	v_mul_f32_e32 v2, 0x42000000, v33
	v_mul_f32_e32 v3, 0x42000000, v29
	v_cvt_pk_fp8_f32 v12, v2, v3 op_sel:[0,0,1]
	ds_write2_b32 v83, v75, v9 offset1:8
	ds_write2_b32 v83, v6, v10 offset0:33 offset1:41
	ds_write2_b32 v83, v8, v11 offset0:66 offset1:74
	ds_write2_b32 v83, v5, v12 offset0:99 offset1:107
	v_mul_f32_e32 v2, 0x42000000, v38
	v_mul_f32_e32 v3, 0x42000000, v34
	v_mov_b32_e32 v6, v71
	v_cvt_pk_fp8_f32 v6, v2, v3
	v_mul_f32_e32 v2, 0x42000000, v39
	v_mul_f32_e32 v3, 0x42000000, v35
	v_mov_b32_e32 v7, v71
	v_cvt_pk_fp8_f32 v7, v2, v3
	v_mul_f32_e32 v2, 0x42000000, v47
	v_mul_f32_e32 v3, 0x42000000, v43
	v_mov_b32_e32 v8, v71
	v_cvt_pk_fp8_f32 v7, v2, v3 op_sel:[0,0,1]
	v_mul_f32_e32 v2, 0x42000000, v40
	v_mul_f32_e32 v3, 0x42000000, v36
	v_cvt_pk_fp8_f32 v8, v2, v3
	v_mul_f32_e32 v2, 0x42000000, v41
	v_mul_f32_e32 v3, 0x42000000, v37
	v_mov_b32_e32 v9, v71
	v_cvt_pk_fp8_f32 v9, v2, v3
	v_mul_f32_e32 v2, 0x42000000, v49
	v_mul_f32_e32 v3, 0x42000000, v45
	v_mov_b32_e32 v10, v71
	v_cvt_pk_fp8_f32 v9, v2, v3 op_sel:[0,0,1]
	v_mul_f32_e32 v2, 0x42000000, v54
	v_mul_f32_e32 v3, 0x42000000, v50
	v_cvt_pk_fp8_f32 v10, v2, v3
	v_mul_f32_e32 v2, 0x42000000, v55
	v_mul_f32_e32 v3, 0x42000000, v51
	v_mov_b32_e32 v11, v71
	v_cvt_pk_fp8_f32 v11, v2, v3
	v_mul_f32_e32 v2, 0x42000000, v63
	v_mul_f32_e32 v3, 0x42000000, v59
	v_mul_f32_e32 v4, 0x42000000, v46
	v_mul_f32_e32 v5, 0x42000000, v42
	v_cvt_pk_fp8_f32 v11, v2, v3 op_sel:[0,0,1]
	v_mul_f32_e32 v2, 0x42000000, v56
	v_mul_f32_e32 v3, 0x42000000, v52
	v_mov_b32_e32 v12, v71
	v_cvt_pk_fp8_f32 v6, v4, v5 op_sel:[0,0,1]
	v_mul_f32_e32 v4, 0x42000000, v48
	v_mul_f32_e32 v5, 0x42000000, v44
	v_cvt_pk_fp8_f32 v12, v2, v3
	v_mul_f32_e32 v2, 0x42000000, v57
	v_mul_f32_e32 v3, 0x42000000, v53
	v_mov_b32_e32 v13, v71
	v_cvt_pk_fp8_f32 v8, v4, v5 op_sel:[0,0,1]
	v_mul_f32_e32 v4, 0x42000000, v62
	v_mul_f32_e32 v5, 0x42000000, v58
	v_cvt_pk_fp8_f32 v13, v2, v3
	v_cvt_pk_fp8_f32 v10, v4, v5 op_sel:[0,0,1]
	v_mul_f32_e32 v4, 0x42000000, v64
	v_mul_f32_e32 v5, 0x42000000, v60
	v_cvt_pk_fp8_f32 v12, v4, v5 op_sel:[0,0,1]
	v_mul_f32_e32 v2, 0x42000000, v65
	v_mul_f32_e32 v3, 0x42000000, v61
	s_mul_hi_i32 s4, s25, 0x280000
	s_mul_i32 s25, s25, 0x280000
	v_cvt_pk_fp8_f32 v13, v2, v3 op_sel:[0,0,1]
	s_add_u32 s5, s37, s25
	ds_write2_b32 v83, v6, v10 offset0:16 offset1:24
	ds_write2_b32 v83, v7, v11 offset0:49 offset1:57
	ds_write2_b32 v83, v8, v12 offset0:82 offset1:90
	ds_write2_b32 v83, v9, v13 offset0:115 offset1:123
	s_addc_u32 s25, s38, s4
	s_waitcnt lgkmcnt(0)
	s_ashr_i32 s51, s24, 31
	s_add_u32 s4, s5, s24
	ds_read2_b32 v[2:3], v84 offset1:1
	ds_read2_b32 v[4:5], v84 offset0:2 offset1:3
	s_addc_u32 s5, s25, s51
	v_or_b32_e32 v6, s22, v1
	v_lshl_add_u64 v[10:11], s[4:5], 0, v[72:73]
	v_lshlrev_b32_e32 v6, 10, v6
	v_mov_b32_e32 v7, v71
	v_lshl_add_u64 v[12:13], v[10:11], 0, v[6:7]
	ds_read2_b32 v[6:7], v85 offset1:1
	ds_read2_b32 v[8:9], v86 offset1:1
	s_waitcnt lgkmcnt(2)
	global_store_dwordx4 v[12:13], v[2:5], off sc1 nt
	s_nop 1
	v_or_b32_e32 v2, s22, v69
	v_lshlrev_b32_e32 v2, 10, v2
	v_mov_b32_e32 v3, v71
	v_lshl_add_u64 v[2:3], v[10:11], 0, v[2:3]
	s_waitcnt lgkmcnt(0)
	global_store_dwordx4 v[2:3], v[6:9], off sc1 nt
	ds_read2_b32 v[2:3], v87 offset1:1
	ds_read2_b32 v[4:5], v88 offset1:1
	v_or_b32_e32 v6, s22, v78
	v_lshlrev_b32_e32 v6, 10, v6
	v_mov_b32_e32 v7, v71
	v_lshl_add_u64 v[12:13], v[10:11], 0, v[6:7]
	ds_read2_b32 v[6:7], v89 offset1:1
	ds_read2_b32 v[8:9], v90 offset1:1
	s_waitcnt lgkmcnt(2)
	global_store_dwordx4 v[12:13], v[2:5], off sc1 nt
	s_nop 1
	v_or_b32_e32 v2, s22, v79
	v_lshlrev_b32_e32 v2, 10, v2
	v_mov_b32_e32 v3, v71
	v_lshl_add_u64 v[2:3], v[10:11], 0, v[2:3]
	s_waitcnt lgkmcnt(0)
	global_store_dwordx4 v[2:3], v[6:9], off sc1 nt
	s_waitcnt lgkmcnt(0)

.LBB0_10:
	s_cmpk_gt_i32 s73, 0x9ff
	s_mov_b64 s[4:5], -1
	s_cbranch_scc0 .LBB0_89
	s_cmpk_gt_u32 s73, 0x1dff
	s_cbranch_scc0 .LBB0_21
	s_cmpk_gt_u32 s73, 0x21ff
	s_cbranch_scc0 .LBB0_18
	s_cmp_gt_u32 s73, 0x121ff
	s_cbranch_scc0 .LBB0_15
	s_add_i32 s4, s73, 0xfffede00
	s_lshr_b32 s22, s4, 8
	s_lshl_b64 s[24:25], s[22:23], 20
	s_lshl_b64 s[4:5], s[22:23], 22
	s_add_u32 s51, s20, s4
	s_addc_u32 s55, s21, s5
	s_add_u32 s5, s15, s24
	s_addc_u32 s22, s17, s25
	s_and_b32 s4, s41, 0x3e0
	s_and_b32 s25, s73, 0xe0
	s_and_b32 s24, s39, 0x380
	v_or_b32_e32 v2, s25, v1
	s_lshl_b32 s25, s4, 2
	s_add_u32 s74, s51, s25
	s_addc_u32 s75, s55, 0
	v_lshlrev_b32_e32 v2, 14, v2
	v_lshl_add_u64 v[4:5], s[74:75], 0, v[70:71]
	v_mov_b32_e32 v3, v71
	v_lshl_add_u64 v[50:51], v[4:5], 0, v[2:3]
	v_add_co_u32_e32 v10, vcc, s47, v50
	global_load_dwordx4 v[2:5], v[50:51], off nt
	s_nop 0
	v_addc_co_u32_e32 v11, vcc, 0, v51, vcc
	v_add_co_u32_e32 v14, vcc, s48, v50
	global_load_dwordx4 v[6:9], v[10:11], off offset:-4096 nt
	s_nop 0
	global_load_dwordx4 v[10:13], v[10:11], off nt
	v_addc_co_u32_e32 v15, vcc, 0, v51, vcc
	v_add_co_u32_e32 v22, vcc, s49, v50
	global_load_dwordx4 v[14:17], v[14:15], off nt
	s_nop 0
	v_addc_co_u32_e32 v23, vcc, 0, v51, vcc
	global_load_dwordx4 v[18:21], v[22:23], off offset:-4096 nt
	s_nop 0
	global_load_dwordx4 v[22:25], v[22:23], off nt
	v_add_co_u32_e32 v30, vcc, s50, v50
	v_mov_b32_e32 v76, v71
	s_nop 0
	v_addc_co_u32_e32 v31, vcc, 0, v51, vcc
	global_load_dwordx4 v[26:29], v[30:31], off offset:-4096 nt
	s_nop 0
	global_load_dwordx4 v[30:33], v[30:31], off nt
	v_add_co_u32_e32 v38, vcc, s53, v50
	v_mov_b32_e32 v77, v71
	s_nop 0
	v_addc_co_u32_e32 v39, vcc, 0, v51, vcc
	v_add_co_u32_e32 v46, vcc, s56, v50
	v_mov_b32_e32 v106, v71
	s_nop 0
	v_addc_co_u32_e32 v47, vcc, 0, v51, vcc
	global_load_dwordx4 v[34:37], v[38:39], off offset:-4096 nt
	s_nop 0
	global_load_dwordx4 v[38:41], v[38:39], off nt
	s_nop 0
	global_load_dwordx4 v[42:45], v[46:47], off offset:-4096 nt
	s_nop 0
	global_load_dwordx4 v[46:49], v[46:47], off nt
	v_add_co_u32_e32 v54, vcc, s57, v50
	v_mov_b32_e32 v75, v71
	s_nop 0
	v_addc_co_u32_e32 v55, vcc, 0, v51, vcc
	v_add_co_u32_e32 v62, vcc, s58, v50
	s_add_u32 s24, s5, s24
	s_nop 0
	v_addc_co_u32_e32 v63, vcc, 0, v51, vcc
	global_load_dwordx4 v[50:53], v[54:55], off offset:-4096 nt
	s_nop 0
	global_load_dwordx4 v[54:57], v[54:55], off nt
	s_nop 0
	global_load_dwordx4 v[58:61], v[62:63], off offset:-4096 nt
	s_nop 0
	global_load_dwordx4 v[62:65], v[62:63], off nt
	s_addc_u32 s25, s22, 0
	s_waitcnt vmcnt(15)
	v_mul_f32_e32 v3, 0x42800000, v3
	v_mul_f32_e32 v4, 0x42800000, v4
	v_mul_f32_e32 v5, 0x42800000, v5
	v_mul_f32_e32 v2, 0x42800000, v2
	s_waitcnt vmcnt(14)
	v_mul_f32_e32 v7, 0x42800000, v7
	v_mul_f32_e32 v8, 0x42800000, v8
	v_mul_f32_e32 v9, 0x42800000, v9
	v_cvt_pk_fp8_f32 v76, v3, v7
	v_cvt_pk_fp8_f32 v77, v4, v8
	v_cvt_pk_fp8_f32 v106, v5, v9
	v_mov_b32_e32 v5, v71
	v_mul_f32_e32 v6, 0x42800000, v6
	s_waitcnt vmcnt(11)
	v_mul_f32_e32 v3, 0x42800000, v19
	s_waitcnt vmcnt(10)
	v_mul_f32_e32 v4, 0x42800000, v23
	v_cvt_pk_fp8_f32 v5, v3, v4
	v_mul_f32_e32 v18, 0x42800000, v18
	v_mul_f32_e32 v22, 0x42800000, v22
	v_cvt_pk_fp8_f32 v75, v2, v6
	v_mov_b32_e32 v2, v71
	v_cvt_pk_fp8_f32 v2, v18, v22
	s_waitcnt vmcnt(9)
	v_mul_f32_e32 v3, 0x42800000, v27
	s_waitcnt vmcnt(8)
	v_mul_f32_e32 v4, 0x42800000, v31
	v_cvt_pk_fp8_f32 v5, v3, v4 op_sel:[0,0,1]
	v_mul_f32_e32 v3, 0x42800000, v20
	v_mul_f32_e32 v4, 0x42800000, v24
	v_mov_b32_e32 v8, v71
	v_cvt_pk_fp8_f32 v8, v3, v4
	v_mul_f32_e32 v3, 0x42800000, v21
	v_mul_f32_e32 v4, 0x42800000, v25
	v_mov_b32_e32 v9, v71
	v_mul_f32_e32 v10, 0x42800000, v10
	v_mul_f32_e32 v14, 0x42800000, v14
	v_mul_f32_e32 v26, 0x42800000, v26
	v_mul_f32_e32 v30, 0x42800000, v30
	v_cvt_pk_fp8_f32 v9, v3, v4
	v_mul_f32_e32 v11, 0x42800000, v11
	v_mul_f32_e32 v15, 0x42800000, v15
	v_cvt_pk_fp8_f32 v75, v10, v14 op_sel:[0,0,1]
	v_cvt_pk_fp8_f32 v2, v26, v30 op_sel:[0,0,1]
	v_mul_f32_e32 v12, 0x42800000, v12
	v_mul_f32_e32 v16, 0x42800000, v16
	v_cvt_pk_fp8_f32 v76, v11, v15 op_sel:[0,0,1]
	v_mul_f32_e32 v6, 0x42800000, v28
	v_mul_f32_e32 v7, 0x42800000, v32
	v_mul_f32_e32 v13, 0x42800000, v13
	v_mul_f32_e32 v17, 0x42800000, v17
	v_cvt_pk_fp8_f32 v77, v12, v16 op_sel:[0,0,1]
	v_cvt_pk_fp8_f32 v8, v6, v7 op_sel:[0,0,1]
	v_mul_f32_e32 v3, 0x42800000, v29
	v_mul_f32_e32 v4, 0x42800000, v33
	v_cvt_pk_fp8_f32 v106, v13, v17 op_sel:[0,0,1]
	v_cvt_pk_fp8_f32 v9, v3, v4 op_sel:[0,0,1]
	ds_write2_b32 v83, v75, v2 offset1:8
	ds_write2_b32 v83, v76, v5 offset0:33 offset1:41
	ds_write2_b32 v83, v77, v8 offset0:66 offset1:74
	ds_write2_b32 v83, v106, v9 offset0:99 offset1:107
	s_waitcnt vmcnt(7)
	v_mul_f32_e32 v2, 0x42800000, v34
	s_waitcnt vmcnt(6)
	v_mul_f32_e32 v3, 0x42800000, v38
	v_mov_b32_e32 v6, v71
	v_cvt_pk_fp8_f32 v6, v2, v3
	v_mul_f32_e32 v2, 0x42800000, v35
	v_mul_f32_e32 v3, 0x42800000, v39
	v_mov_b32_e32 v7, v71
	v_cvt_pk_fp8_f32 v7, v2, v3
	s_waitcnt vmcnt(5)
	v_mul_f32_e32 v2, 0x42800000, v43
	s_waitcnt vmcnt(4)
	v_mul_f32_e32 v3, 0x42800000, v47
	v_mov_b32_e32 v8, v71
	v_cvt_pk_fp8_f32 v7, v2, v3 op_sel:[0,0,1]
	v_mul_f32_e32 v2, 0x42800000, v36
	v_mul_f32_e32 v3, 0x42800000, v40
	v_cvt_pk_fp8_f32 v8, v2, v3
	v_mul_f32_e32 v2, 0x42800000, v37
	v_mul_f32_e32 v3, 0x42800000, v41
	v_mov_b32_e32 v9, v71
	v_cvt_pk_fp8_f32 v9, v2, v3
	v_mul_f32_e32 v2, 0x42800000, v45
	v_mul_f32_e32 v3, 0x42800000, v49
	v_mov_b32_e32 v10, v71
	v_cvt_pk_fp8_f32 v9, v2, v3 op_sel:[0,0,1]
	s_waitcnt vmcnt(3)
	v_mul_f32_e32 v2, 0x42800000, v50
	s_waitcnt vmcnt(2)
	v_mul_f32_e32 v3, 0x42800000, v54
	v_cvt_pk_fp8_f32 v10, v2, v3
	v_mul_f32_e32 v2, 0x42800000, v51
	v_mul_f32_e32 v3, 0x42800000, v55
	v_mov_b32_e32 v11, v71
	v_cvt_pk_fp8_f32 v11, v2, v3
	s_waitcnt vmcnt(1)
	v_mul_f32_e32 v2, 0x42800000, v59
	s_waitcnt vmcnt(0)
	v_mul_f32_e32 v3, 0x42800000, v63
	v_mul_f32_e32 v4, 0x42800000, v42
	v_mul_f32_e32 v5, 0x42800000, v46
	v_cvt_pk_fp8_f32 v11, v2, v3 op_sel:[0,0,1]
	v_mul_f32_e32 v2, 0x42800000, v52
	v_mul_f32_e32 v3, 0x42800000, v56
	v_mov_b32_e32 v12, v71
	v_cvt_pk_fp8_f32 v6, v4, v5 op_sel:[0,0,1]
	v_mul_f32_e32 v4, 0x42800000, v44
	v_mul_f32_e32 v5, 0x42800000, v48
	v_cvt_pk_fp8_f32 v12, v2, v3
	v_mul_f32_e32 v2, 0x42800000, v53
	v_mul_f32_e32 v3, 0x42800000, v57
	v_mov_b32_e32 v13, v71
	v_cvt_pk_fp8_f32 v8, v4, v5 op_sel:[0,0,1]
	v_mul_f32_e32 v4, 0x42800000, v58
	v_mul_f32_e32 v5, 0x42800000, v62
	v_cvt_pk_fp8_f32 v13, v2, v3
	v_cvt_pk_fp8_f32 v10, v4, v5 op_sel:[0,0,1]
	v_mul_f32_e32 v4, 0x42800000, v60
	v_mul_f32_e32 v5, 0x42800000, v64
	v_cvt_pk_fp8_f32 v12, v4, v5 op_sel:[0,0,1]
	v_mul_f32_e32 v2, 0x42800000, v61
	v_mul_f32_e32 v3, 0x42800000, v65
	v_cvt_pk_fp8_f32 v13, v2, v3 op_sel:[0,0,1]
	ds_write2_b32 v83, v6, v10 offset0:16 offset1:24
	ds_write2_b32 v83, v7, v11 offset0:49 offset1:57
	ds_write2_b32 v83, v8, v12 offset0:82 offset1:90
	ds_write2_b32 v83, v9, v13 offset0:115 offset1:123
	s_waitcnt lgkmcnt(0)
	ds_read2_b32 v[2:3], v84 offset1:1
	ds_read2_b32 v[4:5], v84 offset0:2 offset1:3
	v_or_b32_e32 v6, s4, v1
	v_lshl_add_u64 v[10:11], s[24:25], 0, v[72:73]
	v_lshlrev_b32_e32 v6, 10, v6
	v_mov_b32_e32 v7, v71
	v_lshl_add_u64 v[12:13], v[10:11], 0, v[6:7]
	ds_read2_b32 v[6:7], v85 offset1:1
	ds_read2_b32 v[8:9], v86 offset1:1
	s_waitcnt lgkmcnt(2)
	global_store_dwordx4 v[12:13], v[2:5], off sc1 nt
	s_nop 1
	v_or_b32_e32 v2, s4, v69
	v_lshlrev_b32_e32 v2, 10, v2
	v_mov_b32_e32 v3, v71
	v_lshl_add_u64 v[2:3], v[10:11], 0, v[2:3]
	s_waitcnt lgkmcnt(0)
	global_store_dwordx4 v[2:3], v[6:9], off sc1 nt
	ds_read2_b32 v[2:3], v87 offset1:1
	ds_read2_b32 v[4:5], v88 offset1:1
	v_or_b32_e32 v6, s4, v78
	v_lshlrev_b32_e32 v6, 10, v6
	v_mov_b32_e32 v7, v71
	v_lshl_add_u64 v[12:13], v[10:11], 0, v[6:7]
	ds_read2_b32 v[6:7], v89 offset1:1
	ds_read2_b32 v[8:9], v90 offset1:1
	s_waitcnt lgkmcnt(2)
	global_store_dwordx4 v[12:13], v[2:5], off sc1 nt
	s_nop 1
	v_or_b32_e32 v2, s4, v79
	v_lshlrev_b32_e32 v2, 10, v2
	v_mov_b32_e32 v3, v71
	v_lshl_add_u64 v[2:3], v[10:11], 0, v[2:3]
	s_waitcnt lgkmcnt(0)
	global_store_dwordx4 v[2:3], v[6:9], off sc1 nt
	s_waitcnt lgkmcnt(0)
	s_mov_b64 s[4:5], 0
.LBB0_15:
	s_andn2_b64 vcc, exec, s[4:5]
	s_cbranch_vccnz .LBB0_17
	s_add_i32 s4, s73, 0xffffde00
	s_lshr_b32 s22, s4, 9
	s_lshl_b64 s[4:5], s[22:23], 23
	s_add_u32 s24, s18, s4
	s_addc_u32 s25, s19, s5
	s_lshl_b64 s[4:5], s[22:23], 21
	s_add_u32 s4, s26, s4
	s_addc_u32 s5, s27, s5
	s_and_b32 s51, s41, 0x7e0
	s_and_b32 s22, s43, 0x380
	s_lshl_b32 s51, s51, 2
	s_add_u32 s24, s24, s51
	v_or_b32_e32 v4, s22, v67
	s_addc_u32 s25, s25, 0
	v_lshl_add_u64 v[2:3], s[24:25], 0, v[70:71]
	v_lshlrev_b32_e32 v4, 13, v4
	v_mov_b32_e32 v5, v71
	v_lshl_add_u64 v[58:59], v[2:3], 0, v[4:5]
	v_add_co_u32_e32 v6, vcc, s47, v58
	v_mov_b32_e32 v75, v71
	s_nop 0
	v_addc_co_u32_e32 v7, vcc, 0, v59, vcc
	global_load_dwordx4 v[2:5], v[58:59], off nt
	s_nop 0
	global_load_dwordx4 v[6:9], v[6:7], off nt
	v_add_co_u32_e32 v10, vcc, s59, v58
	s_add_u32 s4, s4, s22
	s_nop 0
	v_addc_co_u32_e32 v11, vcc, 0, v59, vcc
	v_add_co_u32_e32 v14, vcc, s60, v58
	s_addc_u32 s5, s5, 0
	s_nop 0
	v_addc_co_u32_e32 v15, vcc, 0, v59, vcc
	global_load_dwordx4 v[10:13], v[10:11], off nt
	s_nop 0
	global_load_dwordx4 v[14:17], v[14:15], off nt
	v_add_co_u32_e32 v18, vcc, s52, v58
	s_waitcnt vmcnt(3)
	v_mul_f32_e32 v2, 0x42000000, v2
	v_addc_co_u32_e32 v19, vcc, 0, v59, vcc
	v_add_co_u32_e32 v22, vcc, s54, v58
	s_waitcnt vmcnt(2)
	v_mul_f32_e32 v6, 0x42000000, v6
	v_addc_co_u32_e32 v23, vcc, 0, v59, vcc
	global_load_dwordx4 v[18:21], v[18:19], off nt
	s_nop 0
	global_load_dwordx4 v[22:25], v[22:23], off nt
	v_add_co_u32_e32 v26, vcc, s61, v58
	v_cvt_pk_fp8_f32 v75, v2, v6
	s_nop 0
	v_addc_co_u32_e32 v27, vcc, 0, v59, vcc
	v_add_co_u32_e32 v30, vcc, s62, v58
	v_mul_f32_e32 v2, 0x42000000, v3
	s_nop 0
	v_addc_co_u32_e32 v31, vcc, 0, v59, vcc
	global_load_dwordx4 v[26:29], v[26:27], off nt
	s_nop 0
	global_load_dwordx4 v[30:33], v[30:31], off nt
	v_add_co_u32_e32 v34, vcc, s63, v58
	v_mul_f32_e32 v3, 0x42000000, v7
	s_nop 0
	v_addc_co_u32_e32 v35, vcc, 0, v59, vcc
	v_add_co_u32_e32 v38, vcc, s64, v58
	v_mov_b32_e32 v6, v71
	s_nop 0
	v_addc_co_u32_e32 v39, vcc, 0, v59, vcc
	global_load_dwordx4 v[34:37], v[34:35], off nt
	s_nop 0
	global_load_dwordx4 v[38:41], v[38:39], off nt
	v_add_co_u32_e32 v42, vcc, s65, v58
	v_cvt_pk_fp8_f32 v6, v2, v3
	s_nop 0
	v_addc_co_u32_e32 v43, vcc, 0, v59, vcc
	v_add_co_u32_e32 v46, vcc, s66, v58
	s_waitcnt vmcnt(7)
	v_mul_f32_e32 v2, 0x42000000, v11
	v_addc_co_u32_e32 v47, vcc, 0, v59, vcc
	global_load_dwordx4 v[42:45], v[42:43], off nt
	s_nop 0
	global_load_dwordx4 v[46:49], v[46:47], off nt
	v_add_co_u32_e32 v50, vcc, s67, v58
	s_waitcnt vmcnt(8)
	v_mul_f32_e32 v3, 0x42000000, v15
	v_addc_co_u32_e32 v51, vcc, 0, v59, vcc
	v_add_co_u32_e32 v54, vcc, s68, v58
	v_cvt_pk_fp8_f32 v6, v2, v3 op_sel:[0,0,1]
	s_nop 0
	v_addc_co_u32_e32 v55, vcc, 0, v59, vcc
	global_load_dwordx4 v[50:53], v[50:51], off nt
	s_nop 0
	global_load_dwordx4 v[54:57], v[54:55], off nt
	v_add_co_u32_e32 v60, vcc, s69, v58
	v_mul_f32_e32 v2, 0x42000000, v4
	s_nop 0
	v_addc_co_u32_e32 v61, vcc, 0, v59, vcc
	v_add_co_u32_e32 v62, vcc, s70, v58
	v_mul_f32_e32 v3, 0x42000000, v8
	s_nop 0
	v_addc_co_u32_e32 v63, vcc, 0, v59, vcc
	global_load_dwordx4 v[58:61], v[60:61], off nt
	s_nop 0
	global_load_dwordx4 v[62:65], v[62:63], off nt
	v_mov_b32_e32 v8, v71
	v_cvt_pk_fp8_f32 v8, v2, v3
	v_mul_f32_e32 v2, 0x42000000, v5
	v_mul_f32_e32 v3, 0x42000000, v9
	v_mov_b32_e32 v5, v71
	v_cvt_pk_fp8_f32 v5, v2, v3
	v_mul_f32_e32 v2, 0x42000000, v13
	v_mul_f32_e32 v3, 0x42000000, v17
	v_mul_f32_e32 v10, 0x42000000, v10
	v_mul_f32_e32 v14, 0x42000000, v14
	v_cvt_pk_fp8_f32 v5, v2, v3 op_sel:[0,0,1]
	v_mov_b32_e32 v9, v71
	v_cvt_pk_fp8_f32 v75, v10, v14 op_sel:[0,0,1]
	v_mov_b32_e32 v10, v71
	v_mov_b32_e32 v11, v71
	v_mul_f32_e32 v4, 0x42000000, v12
	v_mul_f32_e32 v7, 0x42000000, v16
	v_mov_b32_e32 v12, v71
	v_cvt_pk_fp8_f32 v8, v4, v7 op_sel:[0,0,1]
	v_mov_b32_e32 v13, v71
	s_waitcnt vmcnt(11)
	v_mul_f32_e32 v2, 0x42000000, v18
	s_waitcnt vmcnt(10)
	v_mul_f32_e32 v3, 0x42000000, v22
	v_cvt_pk_fp8_f32 v9, v2, v3
	v_mul_f32_e32 v2, 0x42000000, v19
	v_mul_f32_e32 v3, 0x42000000, v23
	v_cvt_pk_fp8_f32 v10, v2, v3
	s_waitcnt vmcnt(9)
	v_mul_f32_e32 v2, 0x42000000, v27
	s_waitcnt vmcnt(8)
	v_mul_f32_e32 v3, 0x42000000, v31
	v_cvt_pk_fp8_f32 v10, v2, v3 op_sel:[0,0,1]
	v_mul_f32_e32 v2, 0x42000000, v20
	v_mul_f32_e32 v3, 0x42000000, v24
	v_cvt_pk_fp8_f32 v11, v2, v3
	v_mul_f32_e32 v2, 0x42000000, v21
	v_mul_f32_e32 v3, 0x42000000, v25
	v_mul_f32_e32 v4, 0x42000000, v26
	v_mul_f32_e32 v7, 0x42000000, v30
	v_cvt_pk_fp8_f32 v12, v2, v3
	v_cvt_pk_fp8_f32 v9, v4, v7 op_sel:[0,0,1]
	v_mul_f32_e32 v4, 0x42000000, v28
	v_mul_f32_e32 v7, 0x42000000, v32
	v_cvt_pk_fp8_f32 v11, v4, v7 op_sel:[0,0,1]
	v_mul_f32_e32 v2, 0x42000000, v29
	v_mul_f32_e32 v3, 0x42000000, v33
	v_cvt_pk_fp8_f32 v12, v2, v3 op_sel:[0,0,1]
	ds_write2_b32 v83, v75, v9 offset1:8
	ds_write2_b32 v83, v6, v10 offset0:33 offset1:41
	ds_write2_b32 v83, v8, v11 offset0:66 offset1:74
	ds_write2_b32 v83, v5, v12 offset0:99 offset1:107
	s_waitcnt vmcnt(7)
	v_mul_f32_e32 v2, 0x42000000, v34
	s_waitcnt vmcnt(6)
	v_mul_f32_e32 v3, 0x42000000, v38
	v_mov_b32_e32 v6, v71
	v_cvt_pk_fp8_f32 v6, v2, v3
	v_mul_f32_e32 v2, 0x42000000, v35
	v_mul_f32_e32 v3, 0x42000000, v39
	v_mov_b32_e32 v7, v71
	v_cvt_pk_fp8_f32 v7, v2, v3
	s_waitcnt vmcnt(5)
	v_mul_f32_e32 v2, 0x42000000, v43
	s_waitcnt vmcnt(4)
	v_mul_f32_e32 v3, 0x42000000, v47
	v_mov_b32_e32 v8, v71
	v_cvt_pk_fp8_f32 v7, v2, v3 op_sel:[0,0,1]
	v_mul_f32_e32 v2, 0x42000000, v36
	v_mul_f32_e32 v3, 0x42000000, v40
	v_cvt_pk_fp8_f32 v8, v2, v3
	v_mul_f32_e32 v2, 0x42000000, v37
	v_mul_f32_e32 v3, 0x42000000, v41
	v_mov_b32_e32 v9, v71
	v_cvt_pk_fp8_f32 v9, v2, v3
	v_mul_f32_e32 v2, 0x42000000, v45
	v_mul_f32_e32 v3, 0x42000000, v49
	v_mov_b32_e32 v10, v71
	v_cvt_pk_fp8_f32 v9, v2, v3 op_sel:[0,0,1]
	s_waitcnt vmcnt(3)
	v_mul_f32_e32 v2, 0x42000000, v50
	s_waitcnt vmcnt(2)
	v_mul_f32_e32 v3, 0x42000000, v54
	v_cvt_pk_fp8_f32 v10, v2, v3
	v_mul_f32_e32 v2, 0x42000000, v51
	v_mul_f32_e32 v3, 0x42000000, v55
	v_mov_b32_e32 v11, v71
	v_cvt_pk_fp8_f32 v11, v2, v3
	s_waitcnt vmcnt(1)
	v_mul_f32_e32 v2, 0x42000000, v59
	s_waitcnt vmcnt(0)
	v_mul_f32_e32 v3, 0x42000000, v63
	v_mul_f32_e32 v4, 0x42000000, v42
	v_mul_f32_e32 v5, 0x42000000, v46
	v_cvt_pk_fp8_f32 v11, v2, v3 op_sel:[0,0,1]
	v_mul_f32_e32 v2, 0x42000000, v52
	v_mul_f32_e32 v3, 0x42000000, v56
	v_mov_b32_e32 v12, v71
	v_cvt_pk_fp8_f32 v6, v4, v5 op_sel:[0,0,1]
	v_mul_f32_e32 v4, 0x42000000, v44
	v_mul_f32_e32 v5, 0x42000000, v48
	v_cvt_pk_fp8_f32 v12, v2, v3
	v_mul_f32_e32 v2, 0x42000000, v53
	v_mul_f32_e32 v3, 0x42000000, v57
	v_cvt_pk_fp8_f32 v8, v4, v5 op_sel:[0,0,1]
	v_mul_f32_e32 v4, 0x42000000, v58
	v_mul_f32_e32 v5, 0x42000000, v62
	v_cvt_pk_fp8_f32 v13, v2, v3
	v_cvt_pk_fp8_f32 v10, v4, v5 op_sel:[0,0,1]
	v_mul_f32_e32 v4, 0x42000000, v60
	v_mul_f32_e32 v5, 0x42000000, v64
	v_cvt_pk_fp8_f32 v12, v4, v5 op_sel:[0,0,1]
	v_mul_f32_e32 v2, 0x42000000, v61
	v_mul_f32_e32 v3, 0x42000000, v65
	v_cvt_pk_fp8_f32 v13, v2, v3 op_sel:[0,0,1]
	ds_write2_b32 v83, v6, v10 offset0:16 offset1:24
	ds_write2_b32 v83, v7, v11 offset0:49 offset1:57
	ds_write2_b32 v83, v8, v12 offset0:82 offset1:90
	ds_write2_b32 v83, v9, v13 offset0:115 offset1:123
	s_waitcnt lgkmcnt(0)
	v_lshl_add_u64 v[10:11], s[4:5], 0, v[72:73]
	s_and_b32 s4, s45, 0x700
	s_and_b32 s5, s39, 0x80
	ds_read2_b32 v[2:3], v84 offset1:1
	ds_read2_b32 v[4:5], v84 offset0:2 offset1:3
	s_or_b32 s4, s4, s5
	s_and_b32 s5, s41, 0x60
	v_or_b32_e32 v6, s5, v1
	v_or_b32_e32 v6, s4, v6
	v_lshlrev_b32_e32 v6, 10, v6
	v_mov_b32_e32 v7, v71
	v_lshl_add_u64 v[12:13], v[10:11], 0, v[6:7]
	ds_read2_b32 v[6:7], v85 offset1:1
	ds_read2_b32 v[8:9], v86 offset1:1
	s_waitcnt lgkmcnt(2)
	global_store_dwordx4 v[12:13], v[2:5], off sc1 nt
	s_nop 1
	v_or_b32_e32 v2, s5, v69
	v_or_b32_e32 v2, s4, v2
	v_lshlrev_b32_e32 v2, 10, v2
	v_mov_b32_e32 v3, v71
	v_lshl_add_u64 v[2:3], v[10:11], 0, v[2:3]
	s_waitcnt lgkmcnt(0)
	global_store_dwordx4 v[2:3], v[6:9], off sc1 nt
	ds_read2_b32 v[2:3], v87 offset1:1
	ds_read2_b32 v[4:5], v88 offset1:1
	v_or_b32_e32 v6, s5, v78
	v_or_b32_e32 v6, s4, v6
	v_lshlrev_b32_e32 v6, 10, v6
	v_mov_b32_e32 v7, v71
	v_lshl_add_u64 v[12:13], v[10:11], 0, v[6:7]
	ds_read2_b32 v[6:7], v89 offset1:1
	ds_read2_b32 v[8:9], v90 offset1:1
	s_waitcnt lgkmcnt(2)
	global_store_dwordx4 v[12:13], v[2:5], off sc1 nt
	s_nop 1
	v_or_b32_e32 v2, s5, v79
	v_or_b32_e32 v2, s4, v2
	v_lshlrev_b32_e32 v2, 10, v2
	v_mov_b32_e32 v3, v71
	v_lshl_add_u64 v[2:3], v[10:11], 0, v[2:3]
	s_waitcnt lgkmcnt(0)
	global_store_dwordx4 v[2:3], v[6:9], off sc1 nt
	s_waitcnt lgkmcnt(0)

.LBB0_18:
	s_andn2_b64 vcc, exec, s[4:5]
	s_cbranch_vccnz .LBB0_20
	s_add_i32 s4, s73, 0xffffe200
	s_lshr_b32 s22, s4, 8
	s_lshl_b64 s[24:25], s[22:23], 20
	s_lshl_b64 s[4:5], s[22:23], 22
	s_add_u32 s51, s8, s4
	s_addc_u32 s55, s9, s5
	s_add_u32 s5, s28, s24
	s_addc_u32 s22, s29, s25
	s_and_b32 s4, s41, 0x3e0
	s_and_b32 s25, s73, 0xe0
	s_and_b32 s24, s39, 0x380
	v_or_b32_e32 v2, s25, v1
	s_lshl_b32 s25, s4, 2
	s_add_u32 s74, s51, s25
	s_addc_u32 s75, s55, 0
	v_lshlrev_b32_e32 v2, 14, v2
	v_lshl_add_u64 v[4:5], s[74:75], 0, v[70:71]
	v_mov_b32_e32 v3, v71
	v_lshl_add_u64 v[50:51], v[4:5], 0, v[2:3]
	v_add_co_u32_e32 v10, vcc, s47, v50
	global_load_dwordx4 v[2:5], v[50:51], off nt
	s_nop 0
	v_addc_co_u32_e32 v11, vcc, 0, v51, vcc
	v_add_co_u32_e32 v14, vcc, s48, v50
	global_load_dwordx4 v[6:9], v[10:11], off offset:-4096 nt
	s_nop 0
	global_load_dwordx4 v[10:13], v[10:11], off nt
	v_addc_co_u32_e32 v15, vcc, 0, v51, vcc
	v_add_co_u32_e32 v22, vcc, s49, v50
	global_load_dwordx4 v[14:17], v[14:15], off nt
	s_nop 0
	v_addc_co_u32_e32 v23, vcc, 0, v51, vcc
	global_load_dwordx4 v[18:21], v[22:23], off offset:-4096 nt
	s_nop 0
	global_load_dwordx4 v[22:25], v[22:23], off nt
	v_add_co_u32_e32 v30, vcc, s50, v50
	v_mov_b32_e32 v76, v71
	s_nop 0
	v_addc_co_u32_e32 v31, vcc, 0, v51, vcc
	global_load_dwordx4 v[26:29], v[30:31], off offset:-4096 nt
	s_nop 0
	global_load_dwordx4 v[30:33], v[30:31], off nt
	v_add_co_u32_e32 v38, vcc, s53, v50
	v_mov_b32_e32 v77, v71
	s_nop 0
	v_addc_co_u32_e32 v39, vcc, 0, v51, vcc
	v_add_co_u32_e32 v46, vcc, s56, v50
	v_mov_b32_e32 v106, v71
	s_nop 0
	v_addc_co_u32_e32 v47, vcc, 0, v51, vcc
	global_load_dwordx4 v[34:37], v[38:39], off offset:-4096 nt
	s_nop 0
	global_load_dwordx4 v[38:41], v[38:39], off nt
	s_nop 0
	global_load_dwordx4 v[42:45], v[46:47], off offset:-4096 nt
	s_nop 0
	global_load_dwordx4 v[46:49], v[46:47], off nt
	v_add_co_u32_e32 v54, vcc, s57, v50
	v_mov_b32_e32 v75, v71
	s_nop 0
	v_addc_co_u32_e32 v55, vcc, 0, v51, vcc
	v_add_co_u32_e32 v62, vcc, s58, v50
	s_add_u32 s24, s5, s24
	s_nop 0
	v_addc_co_u32_e32 v63, vcc, 0, v51, vcc
	global_load_dwordx4 v[50:53], v[54:55], off offset:-4096 nt
	s_nop 0
	global_load_dwordx4 v[54:57], v[54:55], off nt
	s_nop 0
	global_load_dwordx4 v[58:61], v[62:63], off offset:-4096 nt
	s_nop 0
	global_load_dwordx4 v[62:65], v[62:63], off nt
	s_addc_u32 s25, s22, 0
	s_waitcnt vmcnt(15)
	v_mul_f32_e32 v3, 0x42800000, v3
	v_mul_f32_e32 v4, 0x42800000, v4
	v_mul_f32_e32 v5, 0x42800000, v5
	v_mul_f32_e32 v2, 0x42800000, v2
	s_waitcnt vmcnt(14)
	v_mul_f32_e32 v7, 0x42800000, v7
	v_mul_f32_e32 v8, 0x42800000, v8
	v_mul_f32_e32 v9, 0x42800000, v9
	v_cvt_pk_fp8_f32 v76, v3, v7
	v_cvt_pk_fp8_f32 v77, v4, v8
	v_cvt_pk_fp8_f32 v106, v5, v9
	v_mov_b32_e32 v5, v71
	v_mul_f32_e32 v6, 0x42800000, v6
	s_waitcnt vmcnt(11)
	v_mul_f32_e32 v3, 0x42800000, v19
	s_waitcnt vmcnt(10)
	v_mul_f32_e32 v4, 0x42800000, v23
	v_cvt_pk_fp8_f32 v5, v3, v4
	v_mul_f32_e32 v18, 0x42800000, v18
	v_mul_f32_e32 v22, 0x42800000, v22
	v_cvt_pk_fp8_f32 v75, v2, v6
	v_mov_b32_e32 v2, v71
	v_cvt_pk_fp8_f32 v2, v18, v22
	s_waitcnt vmcnt(9)
	v_mul_f32_e32 v3, 0x42800000, v27
	s_waitcnt vmcnt(8)
	v_mul_f32_e32 v4, 0x42800000, v31
	v_cvt_pk_fp8_f32 v5, v3, v4 op_sel:[0,0,1]
	v_mul_f32_e32 v3, 0x42800000, v20
	v_mul_f32_e32 v4, 0x42800000, v24
	v_mov_b32_e32 v8, v71
	v_cvt_pk_fp8_f32 v8, v3, v4
	v_mul_f32_e32 v3, 0x42800000, v21
	v_mul_f32_e32 v4, 0x42800000, v25
	v_mov_b32_e32 v9, v71
	v_mul_f32_e32 v10, 0x42800000, v10
	v_mul_f32_e32 v14, 0x42800000, v14
	v_mul_f32_e32 v26, 0x42800000, v26
	v_mul_f32_e32 v30, 0x42800000, v30
	v_cvt_pk_fp8_f32 v9, v3, v4
	v_mul_f32_e32 v11, 0x42800000, v11
	v_mul_f32_e32 v15, 0x42800000, v15
	v_cvt_pk_fp8_f32 v75, v10, v14 op_sel:[0,0,1]
	v_cvt_pk_fp8_f32 v2, v26, v30 op_sel:[0,0,1]
	v_mul_f32_e32 v12, 0x42800000, v12
	v_mul_f32_e32 v16, 0x42800000, v16
	v_cvt_pk_fp8_f32 v76, v11, v15 op_sel:[0,0,1]
	v_mul_f32_e32 v6, 0x42800000, v28
	v_mul_f32_e32 v7, 0x42800000, v32
	v_mul_f32_e32 v13, 0x42800000, v13
	v_mul_f32_e32 v17, 0x42800000, v17
	v_cvt_pk_fp8_f32 v77, v12, v16 op_sel:[0,0,1]
	v_cvt_pk_fp8_f32 v8, v6, v7 op_sel:[0,0,1]
	v_mul_f32_e32 v3, 0x42800000, v29
	v_mul_f32_e32 v4, 0x42800000, v33
	v_cvt_pk_fp8_f32 v106, v13, v17 op_sel:[0,0,1]
	v_cvt_pk_fp8_f32 v9, v3, v4 op_sel:[0,0,1]
	ds_write2_b32 v83, v75, v2 offset1:8
	ds_write2_b32 v83, v76, v5 offset0:33 offset1:41
	ds_write2_b32 v83, v77, v8 offset0:66 offset1:74
	ds_write2_b32 v83, v106, v9 offset0:99 offset1:107
	s_waitcnt vmcnt(7)
	v_mul_f32_e32 v2, 0x42800000, v34
	s_waitcnt vmcnt(6)
	v_mul_f32_e32 v3, 0x42800000, v38
	v_mov_b32_e32 v6, v71
	v_cvt_pk_fp8_f32 v6, v2, v3
	v_mul_f32_e32 v2, 0x42800000, v35
	v_mul_f32_e32 v3, 0x42800000, v39
	v_mov_b32_e32 v7, v71
	v_cvt_pk_fp8_f32 v7, v2, v3
	s_waitcnt vmcnt(5)
	v_mul_f32_e32 v2, 0x42800000, v43
	s_waitcnt vmcnt(4)
	v_mul_f32_e32 v3, 0x42800000, v47
	v_mov_b32_e32 v8, v71
	v_cvt_pk_fp8_f32 v7, v2, v3 op_sel:[0,0,1]
	v_mul_f32_e32 v2, 0x42800000, v36
	v_mul_f32_e32 v3, 0x42800000, v40
	v_cvt_pk_fp8_f32 v8, v2, v3
	v_mul_f32_e32 v2, 0x42800000, v37
	v_mul_f32_e32 v3, 0x42800000, v41
	v_mov_b32_e32 v9, v71
	v_cvt_pk_fp8_f32 v9, v2, v3
	v_mul_f32_e32 v2, 0x42800000, v45
	v_mul_f32_e32 v3, 0x42800000, v49
	v_mov_b32_e32 v10, v71
	v_cvt_pk_fp8_f32 v9, v2, v3 op_sel:[0,0,1]
	s_waitcnt vmcnt(3)
	v_mul_f32_e32 v2, 0x42800000, v50
	s_waitcnt vmcnt(2)
	v_mul_f32_e32 v3, 0x42800000, v54
	v_cvt_pk_fp8_f32 v10, v2, v3
	v_mul_f32_e32 v2, 0x42800000, v51
	v_mul_f32_e32 v3, 0x42800000, v55
	v_mov_b32_e32 v11, v71
	v_cvt_pk_fp8_f32 v11, v2, v3
	s_waitcnt vmcnt(1)
	v_mul_f32_e32 v2, 0x42800000, v59
	s_waitcnt vmcnt(0)
	v_mul_f32_e32 v3, 0x42800000, v63
	v_mul_f32_e32 v4, 0x42800000, v42
	v_mul_f32_e32 v5, 0x42800000, v46
	v_cvt_pk_fp8_f32 v11, v2, v3 op_sel:[0,0,1]
	v_mul_f32_e32 v2, 0x42800000, v52
	v_mul_f32_e32 v3, 0x42800000, v56
	v_mov_b32_e32 v12, v71
	v_cvt_pk_fp8_f32 v6, v4, v5 op_sel:[0,0,1]
	v_mul_f32_e32 v4, 0x42800000, v44
	v_mul_f32_e32 v5, 0x42800000, v48
	v_cvt_pk_fp8_f32 v12, v2, v3
	v_mul_f32_e32 v2, 0x42800000, v53
	v_mul_f32_e32 v3, 0x42800000, v57
	v_mov_b32_e32 v13, v71
	v_cvt_pk_fp8_f32 v8, v4, v5 op_sel:[0,0,1]
	v_mul_f32_e32 v4, 0x42800000, v58
	v_mul_f32_e32 v5, 0x42800000, v62
	v_cvt_pk_fp8_f32 v13, v2, v3
	v_cvt_pk_fp8_f32 v10, v4, v5 op_sel:[0,0,1]
	v_mul_f32_e32 v4, 0x42800000, v60
	v_mul_f32_e32 v5, 0x42800000, v64
	v_cvt_pk_fp8_f32 v12, v4, v5 op_sel:[0,0,1]
	v_mul_f32_e32 v2, 0x42800000, v61
	v_mul_f32_e32 v3, 0x42800000, v65
	v_cvt_pk_fp8_f32 v13, v2, v3 op_sel:[0,0,1]
	ds_write2_b32 v83, v6, v10 offset0:16 offset1:24
	ds_write2_b32 v83, v7, v11 offset0:49 offset1:57
	ds_write2_b32 v83, v8, v12 offset0:82 offset1:90
	ds_write2_b32 v83, v9, v13 offset0:115 offset1:123
	s_waitcnt lgkmcnt(0)
	ds_read2_b32 v[2:3], v84 offset1:1
	ds_read2_b32 v[4:5], v84 offset0:2 offset1:3
	v_or_b32_e32 v6, s4, v1
	v_lshl_add_u64 v[10:11], s[24:25], 0, v[72:73]
	v_lshlrev_b32_e32 v6, 10, v6
	v_mov_b32_e32 v7, v71
	v_lshl_add_u64 v[12:13], v[10:11], 0, v[6:7]
	ds_read2_b32 v[6:7], v85 offset1:1
	ds_read2_b32 v[8:9], v86 offset1:1
	s_waitcnt lgkmcnt(2)
	global_store_dwordx4 v[12:13], v[2:5], off sc1 nt
	s_nop 1
	v_or_b32_e32 v2, s4, v69
	v_lshlrev_b32_e32 v2, 10, v2
	v_mov_b32_e32 v3, v71
	v_lshl_add_u64 v[2:3], v[10:11], 0, v[2:3]
	s_waitcnt lgkmcnt(0)
	global_store_dwordx4 v[2:3], v[6:9], off sc1 nt
	ds_read2_b32 v[2:3], v87 offset1:1
	ds_read2_b32 v[4:5], v88 offset1:1
	v_or_b32_e32 v6, s4, v78
	v_lshlrev_b32_e32 v6, 10, v6
	v_mov_b32_e32 v7, v71
	v_lshl_add_u64 v[12:13], v[10:11], 0, v[6:7]
	ds_read2_b32 v[6:7], v89 offset1:1
	ds_read2_b32 v[8:9], v90 offset1:1
	s_waitcnt lgkmcnt(2)
	global_store_dwordx4 v[12:13], v[2:5], off sc1 nt
	s_nop 1
	v_or_b32_e32 v2, s4, v79
	v_lshlrev_b32_e32 v2, 10, v2
	v_mov_b32_e32 v3, v71
	v_lshl_add_u64 v[2:3], v[10:11], 0, v[2:3]
	s_waitcnt lgkmcnt(0)
	global_store_dwordx4 v[2:3], v[6:9], off sc1 nt
	s_waitcnt lgkmcnt(0)

.LBB0_87:
	s_or_b64 exec, exec, s[24:25]
	v_add_u32_e32 v2, 0x400, v91
	s_waitcnt vmcnt(0)
	ds_write2_b32 v91, v6, v7 offset1:66
	ds_write2_b32 v91, v9, v8 offset0:132 offset1:198
	ds_write2_b32 v2, v11, v10 offset0:8 offset1:74
	ds_write2_b32 v2, v13, v12 offset0:140 offset1:206
	v_add_u32_e32 v2, 0x800, v91
	ds_write2_b32 v2, v15, v14 offset0:16 offset1:82
	ds_write2_b32 v2, v17, v16 offset0:148 offset1:214
	v_add_u32_e32 v2, 0xc00, v91
	ds_write2_b32 v2, v19, v18 offset0:24 offset1:90
	ds_write2_b32 v2, v21, v20 offset0:156 offset1:222
	v_add_u32_e32 v2, 0x1000, v91
	ds_write2_b32 v2, v23, v22 offset0:32 offset1:98
	ds_write2_b32 v2, v25, v24 offset0:164 offset1:230
	v_add_u32_e32 v2, 0x1400, v91
	ds_write2_b32 v2, v27, v26 offset0:40 offset1:106
	ds_write2_b32 v2, v29, v28 offset0:172 offset1:238
	v_add_u32_e32 v2, 0x1800, v91
	ds_write2_b32 v2, v31, v30 offset0:48 offset1:114
	ds_write2_b32 v2, v33, v32 offset0:180 offset1:246
	v_add_u32_e32 v2, 0x1c00, v91
	s_mul_i32 s74, s74, 0x500000
	ds_write2_b32 v2, v35, v34 offset0:56 offset1:122
	ds_write2_b32 v2, v37, v36 offset0:188 offset1:254
	s_add_u32 s4, s33, s74
	s_waitcnt lgkmcnt(0)
	s_addc_u32 s5, s36, 0
	s_and_b32 s24, 0xffff, s51
	ds_read2_b32 v[6:7], v82 offset0:33 offset1:41
	ds_read2_b32 v[8:9], v82 offset1:8
	ds_read2_b32 v[10:11], v82 offset0:66 offset1:74
	ds_read2_b32 v[12:13], v82 offset0:99 offset1:107
	ds_read2_b32 v[14:15], v82 offset0:132 offset1:140
	ds_read2_b32 v[16:17], v82 offset0:165 offset1:173
	ds_read2_b32 v[18:19], v82 offset0:198 offset1:206
	ds_read2_b32 v[20:21], v82 offset0:231 offset1:239
	s_lshl_b32 s24, s24, 1
	s_add_u32 s4, s4, s24
	s_addc_u32 s5, s5, 0
	v_mov_b32_e32 v75, v71
	s_waitcnt lgkmcnt(6)
	v_cvt_pk_bf16_f32 v2, v8, v6
	v_or_b32_e32 v6, s22, v1
	v_lshl_add_u64 v[22:23], s[4:5], 0, v[74:75]
	v_lshlrev_b32_e32 v24, 11, v6
	v_mov_b32_e32 v25, v71
	s_waitcnt lgkmcnt(4)
	v_cvt_pk_bf16_f32 v3, v10, v12
	s_waitcnt lgkmcnt(2)
	v_cvt_pk_bf16_f32 v4, v14, v16
	s_waitcnt lgkmcnt(0)
	v_cvt_pk_bf16_f32 v5, v18, v20
	v_lshl_add_u64 v[24:25], v[22:23], 0, v[24:25]
	global_store_dwordx4 v[24:25], v[2:5], off sc1 nt
	v_or_b32_e32 v6, s22, v69
	v_lshlrev_b32_e32 v6, 11, v6
	v_cvt_pk_bf16_f32 v2, v9, v7
	v_cvt_pk_bf16_f32 v3, v11, v13
	v_cvt_pk_bf16_f32 v4, v15, v17
	v_cvt_pk_bf16_f32 v5, v19, v21
	ds_read2_b32 v[8:9], v82 offset0:49 offset1:57
	ds_read2_b32 v[10:11], v82 offset0:16 offset1:24
	ds_read2_b32 v[12:13], v82 offset0:82 offset1:90
	ds_read2_b32 v[14:15], v82 offset0:115 offset1:123
	ds_read2_b32 v[16:17], v82 offset0:148 offset1:156
	ds_read2_b32 v[18:19], v82 offset0:181 offset1:189
	ds_read2_b32 v[20:21], v82 offset0:214 offset1:222
	ds_read2_b32 v[24:25], v82 offset0:247 offset1:255
	v_mov_b32_e32 v7, v71
	v_lshl_add_u64 v[6:7], v[22:23], 0, v[6:7]
	global_store_dwordx4 v[6:7], v[2:5], off sc1 nt
	v_or_b32_e32 v6, s22, v78
	v_lshlrev_b32_e32 v6, 11, v6
	v_mov_b32_e32 v7, v71
	s_waitcnt lgkmcnt(6)
	v_cvt_pk_bf16_f32 v2, v10, v8
	s_waitcnt lgkmcnt(4)
	v_cvt_pk_bf16_f32 v3, v12, v14
	s_waitcnt lgkmcnt(2)
	v_cvt_pk_bf16_f32 v4, v16, v18
	s_waitcnt lgkmcnt(0)
	v_cvt_pk_bf16_f32 v5, v20, v24
	v_lshl_add_u64 v[6:7], v[22:23], 0, v[6:7]
	global_store_dwordx4 v[6:7], v[2:5], off sc1 nt
	v_or_b32_e32 v6, s22, v79
	v_lshlrev_b32_e32 v6, 11, v6
	v_mov_b32_e32 v7, v71
	v_cvt_pk_bf16_f32 v2, v11, v9
	v_cvt_pk_bf16_f32 v3, v13, v15
	v_cvt_pk_bf16_f32 v4, v17, v19
	v_cvt_pk_bf16_f32 v5, v21, v25
	v_lshl_add_u64 v[6:7], v[22:23], 0, v[6:7]
	global_store_dwordx4 v[6:7], v[2:5], off sc1 nt
	s_waitcnt lgkmcnt(0)

.LBB0_132:
	v_and_b32_e32 v16, 60, v15
	s_add_i32 s44, s41, s43
	v_add_u32_e32 v20, v13, v15
	v_lshl_add_u32 v16, v16, 2, s42
	v_mov_b32_e32 v48, s44
	v_and_b32_e32 v49, 63, v20
	ds_read_b32 v16, v16 offset:8192
	ds_read_b128 v[20:23], v48
	ds_read_b128 v[24:27], v48 offset:1024
	ds_read_b128 v[28:31], v48 offset:2048
	ds_read_b128 v[32:35], v48 offset:3072
	ds_read_b128 v[36:39], v48 offset:4096
	ds_read_b128 v[40:43], v48 offset:5120
	ds_read_b128 v[44:47], v48 offset:6144
	v_add_u32_e32 v17, v0, v15
	v_add_u32_e32 v19, v12, v15
	v_and_b32_e32 v17, 63, v17
	v_and_b32_e32 v19, 62, v19
	v_lshl_add_u32 v17, v17, 2, s42
	v_lshl_add_u32 v19, v19, 2, s42
	v_lshl_add_u32 v53, v49, 2, s42
	ds_read_b128 v[48:51], v48 offset:7168
	ds_read_b32 v52, v17 offset:8192
	ds_read_b32 v54, v19 offset:8192
	ds_read_b32 v56, v53 offset:8192
	s_waitcnt lgkmcnt(10)
	v_mov_b32_e32 v58, v20
	s_waitcnt lgkmcnt(9)
	v_mov_b32_e32 v59, v24
	s_waitcnt lgkmcnt(8)
	v_mov_b32_e32 v60, v28
	s_waitcnt lgkmcnt(7)
	v_mov_b32_e32 v61, v32
	s_waitcnt lgkmcnt(6)
	v_mov_b32_e32 v62, v36
	s_waitcnt lgkmcnt(5)
	v_mov_b32_e32 v63, v40
	s_waitcnt lgkmcnt(4)
	v_mov_b32_e32 v64, v44
	s_waitcnt lgkmcnt(3)
	v_mov_b32_e32 v65, v48
	v_mov_b32_e32 v24, v21
	v_mov_b32_e32 v32, v29
	v_mov_b32_e32 v40, v37
	v_mov_b32_e32 v48, v45
	v_pk_fma_f32 v[10:11], v[16:17], v[58:59], v[10:11] op_sel_hi:[0,1,1]
	v_pk_fma_f32 v[8:9], v[16:17], v[60:61], v[8:9] op_sel_hi:[0,1,1]
	v_pk_fma_f32 v[6:7], v[16:17], v[62:63], v[6:7] op_sel_hi:[0,1,1]
	v_pk_fma_f32 v[4:5], v[16:17], v[64:65], v[4:5] op_sel_hi:[0,1,1]
	v_mov_b32_e32 v20, v22
	v_mov_b32_e32 v21, v26
	v_mov_b32_e32 v28, v30
	v_mov_b32_e32 v29, v34
	v_mov_b32_e32 v36, v38
	v_mov_b32_e32 v37, v42
	v_mov_b32_e32 v44, v46
	v_mov_b32_e32 v45, v50
	s_waitcnt lgkmcnt(2)
	v_pk_fma_f32 v[10:11], v[52:53], v[24:25], v[10:11] op_sel_hi:[0,1,1]
	v_pk_fma_f32 v[8:9], v[52:53], v[32:33], v[8:9] op_sel_hi:[0,1,1]
	v_pk_fma_f32 v[6:7], v[52:53], v[40:41], v[6:7] op_sel_hi:[0,1,1]
	v_pk_fma_f32 v[4:5], v[52:53], v[48:49], v[4:5] op_sel_hi:[0,1,1]
	s_add_i32 s43, s43, 16
	v_mov_b32_e32 v26, v23
	v_mov_b32_e32 v34, v31
	v_mov_b32_e32 v42, v39
	v_mov_b32_e32 v50, v47
	s_waitcnt lgkmcnt(1)
	v_pk_fma_f32 v[10:11], v[54:55], v[20:21], v[10:11] op_sel_hi:[0,1,1]
	v_pk_fma_f32 v[8:9], v[54:55], v[28:29], v[8:9] op_sel_hi:[0,1,1]
	v_pk_fma_f32 v[6:7], v[54:55], v[36:37], v[6:7] op_sel_hi:[0,1,1]
	v_pk_fma_f32 v[4:5], v[54:55], v[44:45], v[4:5] op_sel_hi:[0,1,1]
	v_add_u32_e32 v15, v15, v1
	s_cmpk_eq_i32 s43, 0x100
	s_waitcnt lgkmcnt(0)
	v_pk_fma_f32 v[10:11], v[56:57], v[26:27], v[10:11] op_sel_hi:[0,1,1]
	v_pk_fma_f32 v[8:9], v[56:57], v[34:35], v[8:9] op_sel_hi:[0,1,1]
	v_pk_fma_f32 v[6:7], v[56:57], v[42:43], v[6:7] op_sel_hi:[0,1,1]
	v_pk_fma_f32 v[4:5], v[56:57], v[50:51], v[4:5] op_sel_hi:[0,1,1]
	s_cbranch_scc0 .LBB0_132
	v_cvt_pk_bf16_f32 v20, v10, v11
	v_cvt_pk_bf16_f32 v21, v8, v9
	v_cvt_pk_bf16_f32 v22, v6, v7
	v_mul_f32_e32 v10, 0x41000000, v10
	v_mul_f32_e32 v11, 0x41000000, v11
	v_mul_f32_e32 v15, 0x41000000, v8
	v_mul_f32_e32 v19, 0x41000000, v9
	v_mov_b32_e32 v8, 0
	v_mul_f32_e32 v6, 0x41000000, v6
	v_mul_f32_e32 v7, 0x41000000, v7
	v_mov_b32_e32 v9, 0
	v_cvt_pk_fp8_f32 v8, v10, v11
	v_cvt_pk_fp8_f32 v9, v6, v7
	s_and_b32 s41, s39, 3
	s_add_u32 s40, s8, s40
	v_cvt_pk_bf16_f32 v23, v4, v5
	s_addc_u32 s42, s9, 0
	s_lshl_b32 s41, s41, 6
	v_mul_f32_e32 v4, 0x41000000, v4
	v_mul_f32_e32 v5, 0x41000000, v5
	s_or_b32 s40, s40, s41
	v_cvt_pk_fp8_f32 v8, v15, v19 op_sel:[0,0,1]
	v_cvt_pk_fp8_f32 v9, v4, v5 op_sel:[0,0,1]
	v_mov_b32_e32 v17, s42
	v_or_b32_e32 v16, s40, v66
	v_lshlrev_b64 v[24:25], 11, v[16:17]
	v_lshlrev_b64 v[4:5], 10, v[16:17]
	s_add_i32 s39, s39, 1
	s_add_i32 s38, s38, 1
	v_lshl_add_u64 v[24:25], s[20:21], 0, v[24:25]
	v_lshl_add_u64 v[4:5], s[22:23], 0, v[4:5]
	s_cmp_eq_u32 s39, 8
	global_store_dwordx4 v[24:25], v[20:23], off sc1 nt
	global_store_dwordx2 v[4:5], v[8:9], off
	s_cbranch_scc0 .LBB0_131
	s_waitcnt lgkmcnt(0)
	s_add_i32 s37, s37, s16
	s_cmpk_gt_i32 s37, 0x1ff
	s_cbranch_scc0 .LBB0_130
